# expert-choice top-k bisection: per-wave candidate count taken from the compare masks with s_bcnt1 instead of a 6-step ds_bpermute butterfly (both layers)
# speedup vs baseline: 1.0003x; 1.0003x over previous
; #define LAS __attribute__((address_space(3)))
; __device__ __forceinline__ void phase_topk(const float* aff, int* SRC, float* GATE, int* INV, int RPE, bool with_ctx, LAS unsigned char* lds) {
;     ...
;             const unsigned cand = thr | (1u << bit);
;             int c = 0;
; #pragma unroll
;             for (int j = 0; j < 8; ++j) c += (vb[j] >= cand) ? 1 : 0;
; #pragma unroll
;             for (int o = 1; o < 64; o <<= 1) c += __shfl_xor(c, o);
;             LAS int* cb = cnts + (bit & 1) * 8;
;             if (lane == 0) cb[wave] = c;
.LBB0_709:
	s_lshl_b32 s50, 1, s52
	v_or_b32_e32 v3, s50, v2
	s_waitcnt vmcnt(0)
	v_cmp_ge_u32_e64 s[56:57], v40, v3
	v_cmp_ge_u32_e64 s[58:59], v41, v3
	v_cmp_ge_u32_e64 s[60:61], v39, v3
	v_cmp_ge_u32_e64 s[62:63], v38, v3
	s_bcnt1_i32_b64 s56, s[56:57]
	s_bcnt1_i32_b64 s58, s[58:59]
	v_cmp_ge_u32_e64 s[64:65], v37, v3
	v_cmp_ge_u32_e64 s[66:67], v36, v3
	s_bcnt1_i32_b64 s60, s[60:61]
	s_bcnt1_i32_b64 s62, s[62:63]
	v_cmp_ge_u32_e64 s[68:69], v35, v3
	v_cmp_ge_u32_e64 s[70:71], v34, v3
	s_bcnt1_i32_b64 s64, s[64:65]
	s_bcnt1_i32_b64 s66, s[66:67]
	s_bcnt1_i32_b64 s68, s[68:69]
	s_bcnt1_i32_b64 s70, s[70:71]
	s_add_i32 s56, s56, s58
	s_add_i32 s60, s60, s62
	s_add_i32 s64, s64, s66
	s_add_i32 s68, s68, s70
	s_add_i32 s56, s56, s60
	s_add_i32 s64, s64, s68
	s_add_i32 s56, s56, s64
	s_and_b32 s50, s53, 8
	s_lshl_b32 s50, s50, 2
	s_add_i32 s54, s50, 0
	v_mov_b32_e32 v4, s56
	v_mov_b32_e32 v5, 0
	s_and_saveexec_b64 s[50:51], vcc
	s_cbranch_execz .LBB0_708
	v_lshl_add_u32 v6, v228, 2, s54
	s_waitcnt lgkmcnt(0)
	v_add_u32_e32 v4, v4, v5
	ds_write_b32 v6, v4 offset:64
	s_branch .LBB0_708

; #define LAS __attribute__((address_space(3)))
; __device__ __forceinline__ void phase_topk(const float* aff, int* SRC, float* GATE, int* INV, int RPE, bool with_ctx, LAS unsigned char* lds) {
;     ...
;             const unsigned cand = thr | (1u << bit);
;             int c = 0;
; #pragma unroll
;             for (int j = 0; j < 8; ++j) c += (vb[j] >= cand) ? 1 : 0;
; #pragma unroll
;             for (int o = 1; o < 64; o <<= 1) c += __shfl_xor(c, o);
;             LAS int* cb = cnts + (bit & 1) * 8;
;             if (lane == 0) cb[wave] = c;
.LBB0_1592:
	s_lshl_b32 s48, 1, s50
	v_or_b32_e32 v3, s48, v2
	s_waitcnt vmcnt(0)
	v_cmp_ge_u32_e64 s[56:57], v39, v3
	v_cmp_ge_u32_e64 s[58:59], v40, v3
	v_cmp_ge_u32_e64 s[60:61], v38, v3
	v_cmp_ge_u32_e64 s[62:63], v37, v3
	s_bcnt1_i32_b64 s56, s[56:57]
	s_bcnt1_i32_b64 s58, s[58:59]
	v_cmp_ge_u32_e64 s[64:65], v36, v3
	v_cmp_ge_u32_e64 s[66:67], v35, v3
	s_bcnt1_i32_b64 s60, s[60:61]
	s_bcnt1_i32_b64 s62, s[62:63]
	v_cmp_ge_u32_e64 s[68:69], v34, v3
	v_cmp_ge_u32_e64 s[70:71], v33, v3
	s_bcnt1_i32_b64 s64, s[64:65]
	s_bcnt1_i32_b64 s66, s[66:67]
	s_bcnt1_i32_b64 s68, s[68:69]
	s_bcnt1_i32_b64 s70, s[70:71]
	s_add_i32 s56, s56, s58
	s_add_i32 s60, s60, s62
	s_add_i32 s64, s64, s66
	s_add_i32 s68, s68, s70
	s_add_i32 s56, s56, s60
	s_add_i32 s64, s64, s68
	s_add_i32 s56, s56, s64
	s_and_b32 s48, s51, 8
	s_lshl_b32 s48, s48, 2
	s_add_i32 s52, s48, 0
	v_mov_b32_e32 v4, s56
	v_mov_b32_e32 v5, 0
	s_and_saveexec_b64 s[48:49], vcc
	s_cbranch_execz .LBB0_1591
	v_lshl_add_u32 v6, v228, 2, s52
	s_waitcnt lgkmcnt(0)
	v_add_u32_e32 v4, v4, v5
	ds_write_b32 v6, v4 offset:64
	s_branch .LBB0_1591
